# adds: attention QK blocks pipeline their K-fragment LDS reads (rolling double buffer; second parity runs the first score chain through four buffers parked in the not-yet-initialised accumulator)
# baseline (speedup 1.0000x reference)
.LBB0_692:
	s_add_i32 s2, s65, 1
	s_cmp_lg_u32 s65, 2
	s_cselect_b32 s47, s2, 0
	s_add_i32 s2, s44, -3
	s_cmp_ge_i32 s2, s70
	s_cbranch_scc1 .LBB0_695
	v_cvt_f32_i32_e32 v0, s45
	s_cmp_lg_u32 s44, 4
	v_fma_f32 v0, v188, v0, v248
	v_sub_f32_e32 v0, v0, v181
	v_pk_add_f32 v[114:115], v[218:219], v[0:1] op_sel_hi:[1,0]
	v_pk_add_f32 v[112:113], v[214:215], v[0:1] op_sel_hi:[1,0]
	v_pk_add_f32 v[110:111], v[210:211], v[0:1] op_sel_hi:[1,0]
	v_pk_add_f32 v[108:109], v[206:207], v[0:1] op_sel_hi:[1,0]
	v_pk_add_f32 v[106:107], v[202:203], v[0:1] op_sel_hi:[1,0]
	v_pk_add_f32 v[104:105], v[198:199], v[0:1] op_sel_hi:[1,0]
	v_pk_add_f32 v[102:103], v[194:195], v[0:1] op_sel_hi:[1,0]
	v_pk_add_f32 v[100:101], v[190:191], v[0:1] op_sel_hi:[1,0]
	v_pk_add_f32 v[130:131], v[220:221], v[0:1] op_sel_hi:[1,0]
	v_pk_add_f32 v[128:129], v[216:217], v[0:1] op_sel_hi:[1,0]
	v_pk_add_f32 v[126:127], v[212:213], v[0:1] op_sel_hi:[1,0]
	v_pk_add_f32 v[124:125], v[208:209], v[0:1] op_sel_hi:[1,0]
	v_pk_add_f32 v[122:123], v[204:205], v[0:1] op_sel_hi:[1,0]
	v_pk_add_f32 v[120:121], v[200:201], v[0:1] op_sel_hi:[1,0]
	v_pk_add_f32 v[118:119], v[196:197], v[0:1] op_sel_hi:[1,0]
	v_pk_add_f32 v[116:117], v[192:193], v[0:1] op_sel_hi:[1,0]
	v_lshl_add_u32 v0, s47, 14, v249
	ds_read_b128 v[132:135], v0
	ds_read_b128 v[136:139], v0 offset:512
	s_waitcnt lgkmcnt(1)
	v_mfma_f32_32x32x16_bf16 v[100:115], v[132:135], v[164:167], v[100:115]
	ds_read_b128 v[132:135], v0 offset:2048
	s_waitcnt lgkmcnt(1)
	v_mfma_f32_32x32x16_bf16 v[116:131], v[136:139], v[164:167], v[116:131]
	ds_read_b128 v[136:139], v0 offset:2560
	s_waitcnt lgkmcnt(1)
	v_mfma_f32_32x32x16_bf16 v[100:115], v[132:135], v[168:171], v[100:115]
	ds_read_b128 v[132:135], v0 offset:4096
	s_waitcnt lgkmcnt(1)
	v_mfma_f32_32x32x16_bf16 v[116:131], v[136:139], v[168:171], v[116:131]
	ds_read_b128 v[136:139], v0 offset:4608
	s_waitcnt lgkmcnt(1)
	v_mfma_f32_32x32x16_bf16 v[100:115], v[132:135], v[172:175], v[100:115]
	ds_read_b128 v[132:135], v0 offset:6144
	s_waitcnt lgkmcnt(1)
	v_mfma_f32_32x32x16_bf16 v[116:131], v[136:139], v[172:175], v[116:131]
	ds_read_b128 v[136:139], v0 offset:6656
	s_waitcnt lgkmcnt(1)
	v_mfma_f32_32x32x16_bf16 v[100:115], v[132:135], v[176:179], v[100:115]
	s_waitcnt lgkmcnt(0)
	v_mfma_f32_32x32x16_bf16 v[116:131], v[136:139], v[176:179], v[116:131]
	s_cbranch_scc1 .LBB0_695
	v_add_u32_e32 v0, s45, v242
	v_add_u32_e32 v132, 32, v0
	v_cmp_le_i32_e32 vcc, v132, v250
	v_add_u32_e32 v132, 33, v0
	s_nop 6
	v_cndmask_b32_e32 v116, v235, v116, vcc
	v_cmp_lt_i32_e32 vcc, v0, v250
	s_nop 1
	v_cndmask_b32_e32 v101, v235, v101, vcc
	v_cmp_le_i32_e32 vcc, v0, v250
	s_nop 1
	v_cndmask_b32_e32 v100, v235, v100, vcc
	v_cmp_le_i32_e32 vcc, v132, v250
	v_add_u32_e32 v132, 2, v0
	s_nop 0
	v_cndmask_b32_e32 v117, v235, v117, vcc
	v_cmp_le_i32_e32 vcc, v132, v250
	v_add_u32_e32 v132, 34, v0
	s_nop 0
	v_cndmask_b32_e32 v102, v235, v102, vcc
	v_cmp_le_i32_e32 vcc, v132, v250
	v_add_u32_e32 v132, 3, v0
	s_nop 0
	v_cndmask_b32_e32 v118, v235, v118, vcc
	v_cmp_le_i32_e32 vcc, v132, v250
	v_add_u32_e32 v132, 35, v0
	s_nop 0
	v_cndmask_b32_e32 v103, v235, v103, vcc
	v_cmp_le_i32_e32 vcc, v132, v250
	v_add_u32_e32 v132, 8, v0
	s_nop 0
	v_cndmask_b32_e32 v119, v235, v119, vcc
	v_cmp_le_i32_e32 vcc, v132, v250
	v_add_u32_e32 v132, 40, v0
	s_nop 0
	v_cndmask_b32_e32 v104, v235, v104, vcc
	v_cmp_le_i32_e32 vcc, v132, v250
	v_add_u32_e32 v132, 9, v0
	s_nop 0
	v_cndmask_b32_e32 v120, v235, v120, vcc
	v_cmp_le_i32_e32 vcc, v132, v250
	v_add_u32_e32 v132, 41, v0
	s_nop 0
	v_cndmask_b32_e32 v105, v235, v105, vcc
	v_cmp_le_i32_e32 vcc, v132, v250
	v_add_u32_e32 v132, 10, v0
	s_nop 0
	v_cndmask_b32_e32 v121, v235, v121, vcc
	v_cmp_le_i32_e32 vcc, v132, v250
	v_add_u32_e32 v132, 42, v0
	s_nop 0
	v_cndmask_b32_e32 v106, v235, v106, vcc
	v_cmp_le_i32_e32 vcc, v132, v250
	v_add_u32_e32 v132, 11, v0
	s_nop 0
	v_cndmask_b32_e32 v122, v235, v122, vcc
	v_cmp_le_i32_e32 vcc, v132, v250
	v_add_u32_e32 v132, 43, v0
	s_nop 0
	v_cndmask_b32_e32 v107, v235, v107, vcc
	v_cmp_le_i32_e32 vcc, v132, v250
	v_add_u32_e32 v132, 16, v0
	s_nop 0
	v_cndmask_b32_e32 v123, v235, v123, vcc
	v_cmp_le_i32_e32 vcc, v132, v250
	v_add_u32_e32 v132, 48, v0
	s_nop 0
	v_cndmask_b32_e32 v108, v235, v108, vcc
	v_cmp_le_i32_e32 vcc, v132, v250
	v_add_u32_e32 v132, 17, v0
	s_nop 0
	v_cndmask_b32_e32 v124, v235, v124, vcc
	v_cmp_le_i32_e32 vcc, v132, v250
	v_add_u32_e32 v132, 49, v0
	s_nop 0
	v_cndmask_b32_e32 v109, v235, v109, vcc
	v_cmp_le_i32_e32 vcc, v132, v250
	v_add_u32_e32 v132, 18, v0
	s_nop 0
	v_cndmask_b32_e32 v125, v235, v125, vcc
	v_cmp_le_i32_e32 vcc, v132, v250
	v_add_u32_e32 v132, 50, v0
	s_nop 0
	v_cndmask_b32_e32 v110, v235, v110, vcc
	v_cmp_le_i32_e32 vcc, v132, v250
	v_add_u32_e32 v132, 19, v0
	s_nop 0
	v_cndmask_b32_e32 v126, v235, v126, vcc
	v_cmp_le_i32_e32 vcc, v132, v250
	v_add_u32_e32 v132, 51, v0
	s_nop 0
	v_cndmask_b32_e32 v111, v235, v111, vcc
	v_cmp_le_i32_e32 vcc, v132, v250
	v_add_u32_e32 v132, 24, v0
	s_nop 0
	v_cndmask_b32_e32 v127, v235, v127, vcc
	v_cmp_le_i32_e32 vcc, v132, v250
	v_add_u32_e32 v132, 56, v0
	s_nop 0
	v_cndmask_b32_e32 v112, v235, v112, vcc
	v_cmp_le_i32_e32 vcc, v132, v250
	v_add_u32_e32 v132, 25, v0
	s_nop 0
	v_cndmask_b32_e32 v128, v235, v128, vcc
	v_cmp_le_i32_e32 vcc, v132, v250
	v_add_u32_e32 v132, 57, v0
	s_nop 0
	v_cndmask_b32_e32 v113, v235, v113, vcc
	v_cmp_le_i32_e32 vcc, v132, v250
	v_add_u32_e32 v132, 26, v0
	s_nop 0
	v_cndmask_b32_e32 v129, v235, v129, vcc
	v_cmp_le_i32_e32 vcc, v132, v250
	v_add_u32_e32 v132, 58, v0
	s_nop 0
	v_cndmask_b32_e32 v114, v235, v114, vcc
	v_cmp_le_i32_e32 vcc, v132, v250
	v_add_u32_e32 v132, 27, v0
	v_add_u32_e32 v0, 59, v0
	v_cndmask_b32_e32 v130, v235, v130, vcc
	v_cmp_le_i32_e32 vcc, v132, v250
	s_nop 1
	v_cndmask_b32_e32 v115, v235, v115, vcc
	v_cmp_le_i32_e32 vcc, v0, v250
	s_nop 1
	v_cndmask_b32_e32 v131, v235, v131, vcc

.LBB0_712:
	s_add_i32 s2, s47, 1
	s_cmp_lg_u32 s47, 2
	s_cselect_b32 s65, s2, 0
	s_andn2_b64 vcc, exec, s[24:25]
	s_cbranch_vccnz .LBB0_714
	v_lshl_add_u32 v226, s65, 14, v249
	ds_read_b128 v[66:69], v226
	ds_read_b128 v[70:73], v226 offset:2048
	ds_read_b128 v[74:77], v226 offset:4096
	ds_read_b128 v[78:81], v226 offset:6144
	ds_read_b128 v[230:233], v226 offset:512
	s_sub_i32 s2, s45, 64
	v_cvt_f32_i32_e32 v0, s2
	v_fma_f32 v0, v188, v0, v248
	v_sub_f32_e32 v0, v0, v183
	v_pk_add_f32 v[96:97], v[218:219], v[0:1] op_sel_hi:[1,0]
	v_pk_add_f32 v[94:95], v[214:215], v[0:1] op_sel_hi:[1,0]
	v_pk_add_f32 v[92:93], v[210:211], v[0:1] op_sel_hi:[1,0]
	v_pk_add_f32 v[90:91], v[206:207], v[0:1] op_sel_hi:[1,0]
	v_pk_add_f32 v[88:89], v[202:203], v[0:1] op_sel_hi:[1,0]
	v_pk_add_f32 v[86:87], v[198:199], v[0:1] op_sel_hi:[1,0]
	v_pk_add_f32 v[84:85], v[194:195], v[0:1] op_sel_hi:[1,0]
	v_pk_add_f32 v[82:83], v[190:191], v[0:1] op_sel_hi:[1,0]
	s_waitcnt lgkmcnt(4)
	s_nop 0
	v_mfma_f32_32x32x16_bf16 v[82:97], v[66:69], v[164:167], v[82:97]
	s_waitcnt lgkmcnt(3)
	v_mfma_f32_32x32x16_bf16 v[82:97], v[70:73], v[168:171], v[82:97]
	s_waitcnt lgkmcnt(2)
	v_mfma_f32_32x32x16_bf16 v[82:97], v[74:77], v[172:175], v[82:97]
	s_waitcnt lgkmcnt(1)
	v_mfma_f32_32x32x16_bf16 v[82:97], v[78:81], v[176:179], v[82:97]
	v_pk_add_f32 v[66:67], v[192:193], v[0:1] op_sel_hi:[1,0]
	v_pk_add_f32 v[68:69], v[196:197], v[0:1] op_sel_hi:[1,0]
	v_pk_add_f32 v[70:71], v[200:201], v[0:1] op_sel_hi:[1,0]
	v_add_f32_e64 v72, v204, v0
	v_add_f32_e64 v73, v205, v0
	v_add_f32_e64 v74, v208, v0
	v_add_f32_e64 v75, v209, v0
	v_add_f32_e64 v76, v212, v0
	v_add_f32_e64 v77, v213, v0
	v_pk_add_f32 v[78:79], v[216:217], v[0:1] op_sel_hi:[1,0]
	v_pk_add_f32 v[80:81], v[220:221], v[0:1] op_sel_hi:[1,0]
	s_waitcnt lgkmcnt(0)
	s_nop 1
	v_mfma_f32_32x32x16_bf16 v[66:81], v[230:233], v[164:167], v[66:81]
	ds_read_b128 v[230:233], v226 offset:2560
	s_waitcnt lgkmcnt(0)
	v_mfma_f32_32x32x16_bf16 v[66:81], v[230:233], v[168:171], v[66:81]
	ds_read_b128 v[230:233], v226 offset:4608
	s_waitcnt lgkmcnt(0)
	v_mfma_f32_32x32x16_bf16 v[66:81], v[230:233], v[172:175], v[66:81]
	ds_read_b128 v[230:233], v226 offset:6656
	s_waitcnt lgkmcnt(0)
	v_mfma_f32_32x32x16_bf16 v[66:81], v[230:233], v[176:179], v[66:81]
	s_branch .LBB0_715
